# attention far-tile loop restructured: K frags prefetched after a moved per-tile barrier, early staging, V reads interleaved with QK MFMAs, global prefetch distance 2
# speedup vs baseline: 1.0001x; 1.0001x over previous
; #define LAS __attribute__((address_space(3)))
; DI kptr_t kargs_now() { kptr_t p = (kptr_t)__builtin_amdgcn_kernarg_segment_ptr(); asm volatile("" : "+s"(p)); return p; }
; DI void refresh(Frame& F) { int w = F.wave; unsigned ones_ = ~0u; asm volatile("" : "+s"(w), "+s"(ones_)); int ln = (int)__builtin_amdgcn_mbcnt_hi(ones_, __builtin_amdgcn_mbcnt_lo(ones_, 0u)); asm volatile("" : "+v"(ln)); F.tid = w * 64 + ln; F.lane = ln; F.wave = w; int b = blockIdx.x; asm volatile("" : "+s"(b)); F.bid = b; }
; #define RI_NEXT(D_) do { if (q.cnt == 8) { int b_ = 0; if (F.lane == 0) b_ = (int)__hip_atomic_fetch_add(qctr, 8u, __ATOMIC_RELAXED, __HIP_MEMORY_SCOPE_AGENT); q.base = __builtin_amdgcn_readfirstlane(b_); q.cnt = 0; } \
;         D_ = decode_item(KA, F.ws, kind, q.base + q.cnt); ++q.cnt; } while (0)
; DI void run_items1(Frame& F, int kind, int quota, QState& q) {
;     const kptr_t KA = kargs_now();
;     LAS float* scr = (LAS float*)(F.lds + F.wave * 16384);
;     unsigned* qctr = F.ctl + CW_QUEUE + 64 * kind;
;     ...
;     if (quota == 0) return;
;     TItem d; RI_NEXT(d); if (!d.valid) return;
; DI void phase_attn(Frame& F, int l) {
;     refresh(F);
;     const kptr_t KA = kargs_now();
;     const bf16_t* qb = (const bf16_t*)(F.ws + WS_Q); const bf16_t* kb = (const bf16_t*)(F.ws + WS_K); const bf16_t* vb = (const bf16_t*)(F.ws + WS_V);
;     const float* kmean = (const float*)(F.ws + WS_KMEAN) + (size_t)l * NB * NBLK * AW; unsigned char* att = F.ws + WS_AZ;
;     constexpr int ATT_BUF = 9216;
;     LAS unsigned char* KS = F.lds; LAS unsigned char* VS = F.lds + 2 * ATT_BUF; LAS float* BIAS = (LAS float*)(F.lds + 4 * ATT_BUF); LAS float* KM = (LAS float*)(F.lds + 4 * ATT_BUF + 512); LAS int* OVF = (LAS int*)(F.lds + 4 * ATT_BUF + 512 + 2048);
;     constexpr int ATT_RC = 208, ATT_RN = 280; LAS float* RT = (LAS float*)(F.lds + 4 * ATT_BUF + 512 + 2048 + 64);
;     QState cq; cq.base = 0; cq.cnt = 8;
;     constexpr int SLOT_ITEMS = 3;
;     if (F.bid & 1) { __syncthreads(); run_items1(F, 1 + l, SLOT_ITEMS, cq); }
.LBB0_398:
	v_readlane_b32 s8, v255, 14
	v_readlane_b32 s4, v253, 8
	s_lshl_b32 s58, s8, 6
	v_readlane_b32 s6, v253, 10
	v_readlane_b32 s7, v253, 11
	s_lshl_b64 s[0:1], s[58:59], 2
	s_mov_b64 s[2:3], s[6:7]
	s_add_u32 s0, s2, s0
	s_addc_u32 s1, s3, s1
	v_readlane_b32 s9, v255, 15
	s_add_u32 s12, s0, 0x8100
	s_addc_u32 s13, s1, 0
	s_lshl_b64 s[0:1], s[8:9], 25
	v_writelane_b32 v255, s0, 16
	s_lshl_b64 s[62:63], s[8:9], 5
	s_lshl_b32 s2, s8, 20
	v_writelane_b32 v255, s1, 17
	s_mov_b32 s3, s59
	v_readlane_b32 s0, v253, 33
	v_writelane_b32 v255, s2, 18
	s_add_u32 s76, s0, s2
	v_readlane_b32 s0, v253, 34
	v_writelane_b32 v255, s3, 19
	s_addc_u32 s77, s0, 0
	s_lshl_b64 s[20:21], s[8:9], 21
	s_lshl_b64 s[0:1], s[8:9], 20
	v_readlane_b32 s2, v253, 35
	s_add_u32 s22, s2, s0
	v_readlane_b32 s2, v253, 36
	s_addc_u32 s23, s2, s1
	v_readlane_b32 s2, v253, 37
	s_add_u32 s24, s2, s0
	v_readlane_b32 s0, v253, 38
	s_addc_u32 s25, s0, s1
	s_lshl_b64 s[26:27], s[8:9], 24
	v_readlane_b32 s0, v253, 39
	s_add_u32 s14, s0, s44
	v_readlane_b32 s0, v253, 40
	s_addc_u32 s15, s0, s45
	s_mov_b32 s0, -1
	s_mov_b32 s95, 0
	v_mbcnt_lo_u32_b32 v0, s0, 0
	v_mbcnt_hi_u32_b32 v186, s0, v0
	v_readlane_b32 s0, v253, 29
	s_mov_b32 s51, s0
	s_mov_b64 s[30:31], s[70:71]
	s_bitcmp0_b32 s51, 0
	s_mov_b32 s63, 8
	v_readlane_b32 s5, v253, 9
	v_readlane_b32 s1, v253, 30
	s_cbranch_scc1 .LBB0_472
	s_mov_b64 s[6:7], s[70:71]
	v_mov_b32_e32 v0, 0
	v_cmp_eq_u32_e64 s[4:5], 0, v186
	s_waitcnt vmcnt(63) expcnt(7) lgkmcnt(15)
	s_barrier
	s_and_saveexec_b64 s[2:3], s[4:5]
	s_cbranch_execz .LBB0_403
	s_mov_b64 s[10:11], exec
	v_mbcnt_lo_u32_b32 v0, s10, 0
	v_mbcnt_hi_u32_b32 v0, s11, v0
	v_cmp_eq_u32_e32 vcc, 0, v0
	s_and_saveexec_b64 s[8:9], vcc
	s_cbranch_execz .LBB0_402
	s_bcnt1_i32_b64 s0, s[10:11]
	s_lshl_b32 s0, s0, 3
	v_mov_b32_e32 v2, s0
	global_atomic_add v2, v1, v2, s[12:13] sc0

; #define LAS __attribute__((address_space(3)))
; DI const float* inp(kptr_t k, int i) { return (const float*)k[i]; }
; DI void phase_attn(Frame& F, int l) {
;     ...
;         { const size_t tok = (size_t)b * SEQ + qblk * 256 + srow; kreg = *(const u32x4*)(kb + tok * AW + h * HD + sch * 8); vreg = *(const u32x4*)(vb + tok * AW + h * HD + sch * 8); }
;         const float km_v = kmean[((size_t)(b * NBLK + (F.tid >> 6))) * AW + h * HD + (F.tid & 63)] * (1.0f / 256.0f);
;         const float bias_v = inp(KA, I_RELB)[t5_bucket(F.tid & 127) * NH + h] * LOG2E;
;         __syncthreads();
;         if (F.tid < 128) BIAS[F.tid] = bias_v;
;         if (F.tid == 0) OVF[0] = 0;
;         KM[F.tid] = km_v;
;         *(LAS u32x4*)(KS + srow * 144 + sch * 16) = kreg; *(LAS u32x4*)(VS + srow * 144 + sch * 16) = vreg;
;         { const size_t tok = (size_t)b * SEQ + qblk * 256 + 64 + srow; kreg = *(const u32x4*)(kb + tok * AW + h * HD + sch * 8); vreg = *(const u32x4*)(vb + tok * AW + h * HD + sch * 8); }
;         __syncthreads();
;         for (int e = F.tid; e < 4 * ATT_RN; e += 512) { const int cpy = e / ATT_RN, dist = ATT_RC - (e - cpy * ATT_RN + cpy); RT[e] = dist < 0 ? -1.0e30f : BIAS[dist > 127 ? 127 : dist]; }
.LBB0_483:
	s_or_b64 exec, exec, s[2:3]
	v_cmp_eq_u32_e32 vcc, 0, v17
	s_and_saveexec_b64 s[2:3], vcc
	ds_write_b32 v1, v1 offset:39424
	s_or_b64 exec, exec, s[2:3]
	s_lshl_b32 s58, s1, 6
	s_waitcnt vmcnt(1)
	v_mul_f32_e32 v19, 0x3b800000, v19
	s_movk_i32 s1, 0x90
	ds_write_b32 v20, v19 offset:37376
	v_mul_lo_u32 v19, v10, s1
	v_lshlrev_b32_e32 v18, 3, v18
	v_add3_u32 v189, 0, v19, v0
	s_lshl_b32 s28, s58, 1
	s_mov_b32 s29, s59
	ds_write_b128 v189, v[2:5]
	ds_write_b128 v189, v[6:9] offset:18432
	v_lshl_add_u64 v[2:3], v[14:15], 0, s[28:29]
	v_lshlrev_b32_e32 v0, 1, v18
	v_lshl_add_u64 v[2:3], v[2:3], 0, v[0:1]
	s_mov_b32 s1, 0x10000
	v_add_co_u32_e32 v4, vcc, s1, v2
	s_movk_i32 s1, 0x460
	s_nop 0
	v_addc_co_u32_e32 v5, vcc, 0, v3, vcc
	global_load_dwordx4 v[160:163], v[4:5], off
	v_lshl_add_u64 v[4:5], v[12:13], 0, s[28:29]
	v_lshl_add_u64 v[4:5], v[4:5], 0, v[0:1]
	v_add_co_u32_e32 v6, vcc, 0x10000, v4
	s_nop 1
	v_addc_co_u32_e32 v7, vcc, 0, v5, vcc
	global_load_dwordx4 v[164:167], v[6:7], off
	s_mov_b64 s[100:101], 0x20000
	v_lshl_add_u64 v[8:9], v[2:3], 0, s[100:101]
	global_load_dwordx4 v[206:209], v[8:9], off
	v_lshl_add_u64 v[8:9], v[4:5], 0, s[100:101]
	global_load_dwordx4 v[210:213], v[8:9], off
	v_cmp_gt_i32_e32 vcc, s1, v17
	s_waitcnt lgkmcnt(0)
	s_barrier
	s_and_saveexec_b64 s[2:3], vcc
	s_cbranch_execz .LBB0_490
	s_lshl_b32 s1, s97, 8
	s_add_i32 s1, s1, 0
	s_add_i32 s1, s1, 0x9a40
	v_add_u32_e32 v7, s0, v186
	v_lshl_add_u32 v6, v186, 2, s1
	v_sub_u32_e32 v7, 0xd0, v7
	s_mov_b64 s[4:5], 0
	s_branch .LBB0_488

; DI float half_sum(float v) { const auto rr = __builtin_amdgcn_permlane32_swap(__float_as_uint(v), __float_as_uint(v), false, false); return __uint_as_float(rr[0]) + __uint_as_float(rr[1]); }
; DI void phase_attn(Frame& F, int l) {
;     ...
;         const float bfar = BIAS[127];
;         unsigned selmask = 0;
;         {
;             float gsc[8];
; #pragma unroll
;             for (int j = 0; j < 8; ++j) { float a = 0.f;
; #pragma unroll
;                 for (int s = 0; s < 4; ++s)
; #pragma unroll
;                     for (int e = 0; e < 8; ++e) a += __uint_as_float(((unsigned)(unsigned short)qf[s][e]) << 16) * KM[j * 64 + 16 * s + 8 * hh + e];
;                 a = half_sum(a); gsc[j] = (j < qblk) ? a : -INFINITY; }
.LBB0_490:
	s_or_b64 exec, exec, s[2:3]
	v_lshl_add_u64 v[182:183], v[2:3], 0, s[74:75]
	v_and_b32_e32 v2, 0xffffffe0, v186
	v_lshl_add_u64 v[184:185], v[4:5], 0, s[74:75]
	v_add_u32_e32 v17, 0, v2
	ds_read_b32 v192, v1 offset:37372
	ds_read_b128 v[2:5], v17 offset:37376
	v_lshlrev_b32_e32 v18, 16, v156
	ds_read_b128 v[6:9], v17 offset:37392
	v_and_b32_e32 v19, 0xffff0000, v156
	v_lshlrev_b32_e32 v20, 16, v157
	s_waitcnt lgkmcnt(1)
	v_fma_f32 v44, v2, v18, 0
	v_fmac_f32_e32 v44, v3, v19
	v_fmac_f32_e32 v44, v4, v20
	s_waitcnt vmcnt(4)
	v_and_b32_e32 v21, 0xffff0000, v157
	v_fmac_f32_e32 v44, v5, v21
	v_lshlrev_b32_e32 v22, 16, v158
	ds_read_b128 v[2:5], v17 offset:37440
	s_waitcnt lgkmcnt(1)
	v_fmac_f32_e32 v44, v6, v22
	v_and_b32_e32 v23, 0xffff0000, v158
	v_fmac_f32_e32 v44, v7, v23
	v_lshlrev_b32_e32 v24, 16, v159
	v_fmac_f32_e32 v44, v8, v24
	v_and_b32_e32 v25, 0xffff0000, v159
	v_fmac_f32_e32 v44, v9, v25
	v_lshlrev_b32_e32 v26, 16, v152
	ds_read_b128 v[6:9], v17 offset:37456
	s_waitcnt lgkmcnt(1)
	v_fmac_f32_e32 v44, v2, v26
	v_and_b32_e32 v27, 0xffff0000, v152
	v_fmac_f32_e32 v44, v3, v27
	v_lshlrev_b32_e32 v28, 16, v153
	v_fmac_f32_e32 v44, v4, v28
	v_and_b32_e32 v29, 0xffff0000, v153
	v_fmac_f32_e32 v44, v5, v29
	v_lshlrev_b32_e32 v30, 16, v154
	ds_read_b128 v[2:5], v17 offset:37504
	s_waitcnt lgkmcnt(1)
	v_fmac_f32_e32 v44, v6, v30
	v_and_b32_e32 v31, 0xffff0000, v154
	v_fmac_f32_e32 v44, v7, v31
	v_lshlrev_b32_e32 v32, 16, v155
	v_fmac_f32_e32 v44, v8, v32
	v_and_b32_e32 v33, 0xffff0000, v155
	v_fmac_f32_e32 v44, v9, v33
	v_lshlrev_b32_e32 v34, 16, v148
	ds_read_b128 v[12:15], v17 offset:37520
	ds_read_b128 v[6:9], v17 offset:37568
	s_waitcnt lgkmcnt(2)
	v_fmac_f32_e32 v44, v2, v34
	v_and_b32_e32 v35, 0xffff0000, v148
	v_fmac_f32_e32 v44, v3, v35
	v_lshlrev_b32_e32 v36, 16, v149
	v_fmac_f32_e32 v44, v4, v36
	v_and_b32_e32 v37, 0xffff0000, v149
	v_fmac_f32_e32 v44, v5, v37
	v_lshlrev_b32_e32 v38, 16, v150
	s_waitcnt lgkmcnt(1)
	v_fmac_f32_e32 v44, v12, v38
	v_and_b32_e32 v39, 0xffff0000, v150
	v_fmac_f32_e32 v44, v13, v39
	v_lshlrev_b32_e32 v40, 16, v151
	v_fmac_f32_e32 v44, v14, v40
	v_and_b32_e32 v41, 0xffff0000, v151
	ds_read_b128 v[2:5], v17 offset:37632
	ds_read_b128 v[46:49], v17 offset:37584
	v_fmac_f32_e32 v44, v15, v41
	v_lshlrev_b32_e32 v42, 16, v144
	s_waitcnt lgkmcnt(2)
	v_fmac_f32_e32 v44, v6, v42
	v_and_b32_e32 v43, 0xffff0000, v144
	v_and_b32_e32 v15, 0xffff0000, v145
	v_lshlrev_b32_e32 v14, 16, v145
	v_fmac_f32_e32 v44, v7, v43
	v_pk_mul_f32 v[8:9], v[8:9], v[14:15]
	v_and_b32_e32 v13, 0xffff0000, v146
	v_lshlrev_b32_e32 v12, 16, v146
	v_add_f32_e32 v8, v44, v8
	s_waitcnt lgkmcnt(0)
	v_pk_mul_f32 v[46:47], v[46:47], v[12:13]
	v_add_f32_e32 v8, v8, v9
	v_and_b32_e32 v7, 0xffff0000, v147
	v_lshlrev_b32_e32 v6, 16, v147
	v_add_f32_e32 v8, v8, v46
	v_add_f32_e32 v44, v8, v47
	v_pk_mul_f32 v[8:9], v[48:49], v[6:7]
	s_cmp_lg_u32 s37, 0
	v_add_f32_e32 v8, v44, v8
	v_add_f32_e32 v8, v8, v9
	v_mov_b32_e32 v9, v8
	s_nop 1
	v_permlane32_swap_b32_e32 v8, v9
	ds_read_b128 v[44:47], v17 offset:37648
	v_add_f32_e32 v64, v8, v9
	v_fma_f32 v8, v2, v18, 0
	v_fmac_f32_e32 v8, v3, v19
	v_fmac_f32_e32 v8, v4, v20
	v_fmac_f32_e32 v8, v5, v21
	ds_read_b128 v[2:5], v17 offset:37696
	s_waitcnt lgkmcnt(1)
	v_fmac_f32_e32 v8, v44, v22
	v_fmac_f32_e32 v8, v45, v23
	v_fmac_f32_e32 v8, v46, v24
	v_fmac_f32_e32 v8, v47, v25
	ds_read_b128 v[44:47], v17 offset:37712
	s_waitcnt lgkmcnt(1)
	v_fmac_f32_e32 v8, v2, v26
	v_fmac_f32_e32 v8, v3, v27
	v_fmac_f32_e32 v8, v4, v28
	v_fmac_f32_e32 v8, v5, v29
	ds_read_b128 v[2:5], v17 offset:37760
	s_waitcnt lgkmcnt(1)
	v_fmac_f32_e32 v8, v44, v30
	v_fmac_f32_e32 v8, v45, v31
	v_fmac_f32_e32 v8, v46, v32
	v_fmac_f32_e32 v8, v47, v33
	ds_read_b128 v[44:47], v17 offset:37776
	s_waitcnt lgkmcnt(1)
	v_fmac_f32_e32 v8, v2, v34
	v_fmac_f32_e32 v8, v3, v35
	v_fmac_f32_e32 v8, v4, v36
	v_fmac_f32_e32 v8, v5, v37
	ds_read_b128 v[2:5], v17 offset:37824
	s_waitcnt lgkmcnt(1)
	v_fmac_f32_e32 v8, v44, v38
	v_fmac_f32_e32 v8, v45, v39
	v_fmac_f32_e32 v8, v46, v40
	ds_read_b128 v[48:51], v17 offset:37888
	ds_read_b128 v[52:55], v17 offset:37840
	v_fmac_f32_e32 v8, v47, v41
	s_waitcnt lgkmcnt(2)
	v_fmac_f32_e32 v8, v2, v42
	v_fmac_f32_e32 v8, v3, v43
	v_pk_mul_f32 v[4:5], v[4:5], v[14:15]
	s_waitcnt lgkmcnt(0)
	v_pk_mul_f32 v[2:3], v[52:53], v[12:13]
	v_add_f32_e32 v4, v8, v4
	v_add_f32_e32 v4, v4, v5
	v_add_f32_e32 v2, v4, v2
	v_add_f32_e32 v4, v2, v3
	v_pk_mul_f32 v[2:3], v[54:55], v[6:7]
	v_fma_f32 v52, v48, v18, 0
	v_add_f32_e32 v2, v4, v2
	v_add_f32_e32 v2, v2, v3
	v_mov_b32_e32 v3, v2
	s_nop 1
	v_permlane32_swap_b32_e32 v2, v3
	v_add_f32_e32 v65, v2, v3
	ds_read_b128 v[2:5], v17 offset:37904
	ds_read_b128 v[44:47], v17 offset:37952
	v_fmac_f32_e32 v52, v49, v19
	v_fmac_f32_e32 v52, v50, v20
	v_fmac_f32_e32 v52, v51, v21
	s_waitcnt lgkmcnt(1)
	v_fmac_f32_e32 v52, v2, v22
	v_fmac_f32_e32 v52, v3, v23
	v_fmac_f32_e32 v52, v4, v24
	v_fmac_f32_e32 v52, v5, v25
	ds_read_b128 v[2:5], v17 offset:37968
	s_waitcnt lgkmcnt(1)
	v_fmac_f32_e32 v52, v44, v26
	v_fmac_f32_e32 v52, v45, v27
	v_fmac_f32_e32 v52, v46, v28
	v_fmac_f32_e32 v52, v47, v29
	ds_read_b128 v[44:47], v17 offset:38016
	s_waitcnt lgkmcnt(1)
	v_fmac_f32_e32 v52, v2, v30
	v_fmac_f32_e32 v52, v3, v31
	v_fmac_f32_e32 v52, v4, v32
	v_fmac_f32_e32 v52, v5, v33
	ds_read_b128 v[2:5], v17 offset:38032
	s_waitcnt lgkmcnt(1)
	v_fmac_f32_e32 v52, v44, v34
	v_fmac_f32_e32 v52, v45, v35
	v_fmac_f32_e32 v52, v46, v36
	v_fmac_f32_e32 v52, v47, v37
	ds_read_b128 v[44:47], v17 offset:38080
	s_waitcnt lgkmcnt(1)
; DI float half_sum(float v) { const auto rr = __builtin_amdgcn_permlane32_swap(__float_as_uint(v), __float_as_uint(v), false, false); return __uint_as_float(rr[0]) + __uint_as_float(rr[1]); }
; DI void phase_attn(Frame& F, int l) {
;     ...
; #pragma unroll
;             for (int j = 0; j < 8; ++j) { float a = 0.f;
; #pragma unroll
;                 for (int s = 0; s < 4; ++s)
; #pragma unroll
;                     for (int e = 0; e < 8; ++e) a += __uint_as_float(((unsigned)(unsigned short)qf[s][e]) << 16) * KM[j * 64 + 16 * s + 8 * hh + e];
;                 a = half_sum(a); gsc[j] = (j < qblk) ? a : -INFINITY; }
	v_fmac_f32_e32 v52, v2, v38
	v_fmac_f32_e32 v52, v3, v39
	v_fmac_f32_e32 v52, v4, v40
	v_fmac_f32_e32 v52, v5, v41
	ds_read_b128 v[2:5], v17 offset:38144
	ds_read_b128 v[48:51], v17 offset:38096
	s_waitcnt lgkmcnt(2)
	v_fmac_f32_e32 v52, v44, v42
	v_fmac_f32_e32 v52, v45, v43
	v_pk_mul_f32 v[8:9], v[46:47], v[14:15]
	s_cselect_b64 s[4:5], -1, 0
	v_add_f32_e32 v8, v52, v8
	v_add_f32_e32 v44, v8, v9
	s_waitcnt lgkmcnt(0)
	v_pk_mul_f32 v[8:9], v[48:49], v[12:13]
	s_cmp_gt_u32 s37, 1
	v_add_f32_e32 v8, v44, v8
	v_add_f32_e32 v44, v8, v9
	v_pk_mul_f32 v[8:9], v[50:51], v[6:7]
	s_cselect_b64 vcc, -1, 0
	v_add_f32_e32 v8, v44, v8
	v_add_f32_e32 v8, v8, v9
	v_mov_b32_e32 v9, v8
	s_nop 1
	v_permlane32_swap_b32_e32 v8, v9
	ds_read_b128 v[44:47], v17 offset:38160
	v_add_f32_e32 v66, v8, v9
	v_fma_f32 v8, v2, v18, 0
	v_fmac_f32_e32 v8, v3, v19
	v_fmac_f32_e32 v8, v4, v20
	v_fmac_f32_e32 v8, v5, v21
	ds_read_b128 v[2:5], v17 offset:38208
	s_waitcnt lgkmcnt(1)
	v_fmac_f32_e32 v8, v44, v22
	v_fmac_f32_e32 v8, v45, v23
	v_fmac_f32_e32 v8, v46, v24
	v_fmac_f32_e32 v8, v47, v25
	ds_read_b128 v[44:47], v17 offset:38224
	s_waitcnt lgkmcnt(1)
	v_fmac_f32_e32 v8, v2, v26
	v_fmac_f32_e32 v8, v3, v27
	v_fmac_f32_e32 v8, v4, v28
	v_fmac_f32_e32 v8, v5, v29
	ds_read_b128 v[2:5], v17 offset:38272
	s_waitcnt lgkmcnt(1)
	v_fmac_f32_e32 v8, v44, v30
	v_fmac_f32_e32 v8, v45, v31
	v_fmac_f32_e32 v8, v46, v32
	v_fmac_f32_e32 v8, v47, v33
	ds_read_b128 v[44:47], v17 offset:38288
	s_waitcnt lgkmcnt(1)
	v_fmac_f32_e32 v8, v2, v34
	v_fmac_f32_e32 v8, v3, v35
	v_fmac_f32_e32 v8, v4, v36
	v_fmac_f32_e32 v8, v5, v37
	ds_read_b128 v[2:5], v17 offset:38336
	s_waitcnt lgkmcnt(1)
	v_fmac_f32_e32 v8, v44, v38
	v_fmac_f32_e32 v8, v45, v39
	v_fmac_f32_e32 v8, v46, v40
	v_fmac_f32_e32 v8, v47, v41
	ds_read_b128 v[44:47], v17 offset:38400
	ds_read_b128 v[48:51], v17 offset:38352
	s_waitcnt lgkmcnt(2)
	v_fmac_f32_e32 v8, v2, v42
	v_fmac_f32_e32 v8, v3, v43
	v_pk_mul_f32 v[2:3], v[4:5], v[14:15]
	ds_read_b128 v[52:55], v17 offset:38672
	v_add_f32_e32 v2, v8, v2
	v_add_f32_e32 v4, v2, v3
	s_waitcnt lgkmcnt(1)
	v_pk_mul_f32 v[2:3], v[48:49], v[12:13]
	v_fma_f32 v8, v44, v18, 0
	v_add_f32_e32 v2, v4, v2
	v_add_f32_e32 v4, v2, v3
	v_pk_mul_f32 v[2:3], v[50:51], v[6:7]
	v_fmac_f32_e32 v8, v45, v19
	v_add_f32_e32 v2, v4, v2
	v_add_f32_e32 v2, v2, v3
	v_mov_b32_e32 v3, v2
	s_nop 1
	v_permlane32_swap_b32_e32 v2, v3
	v_add_f32_e32 v67, v2, v3
	ds_read_b128 v[2:5], v17 offset:38416
	v_fmac_f32_e32 v8, v46, v20
	v_fmac_f32_e32 v8, v47, v21
	ds_read_b128 v[44:47], v17 offset:38464
	ds_read_b128 v[48:51], v17 offset:38608
	s_waitcnt lgkmcnt(2)
	v_fmac_f32_e32 v8, v2, v22
	v_fmac_f32_e32 v8, v3, v23
	v_fmac_f32_e32 v8, v4, v24
	v_fmac_f32_e32 v8, v5, v25
	ds_read_b128 v[2:5], v17 offset:38480
	s_waitcnt lgkmcnt(2)
	v_fmac_f32_e32 v8, v44, v26
	v_fmac_f32_e32 v8, v45, v27
	v_fmac_f32_e32 v8, v46, v28
	v_fmac_f32_e32 v8, v47, v29
	ds_read_b128 v[44:47], v17 offset:38528
	s_waitcnt lgkmcnt(1)
	v_fmac_f32_e32 v8, v2, v30
	v_fmac_f32_e32 v8, v3, v31
	v_fmac_f32_e32 v8, v4, v32
	v_fmac_f32_e32 v8, v5, v33
	ds_read_b128 v[2:5], v17 offset:38544
	s_waitcnt lgkmcnt(1)
	v_fmac_f32_e32 v8, v44, v34
	v_fmac_f32_e32 v8, v45, v35
	v_fmac_f32_e32 v8, v46, v36
	v_fmac_f32_e32 v8, v47, v37
	ds_read_b128 v[44:47], v17 offset:38592
	s_waitcnt lgkmcnt(1)
	v_fmac_f32_e32 v8, v2, v38
	v_fmac_f32_e32 v8, v3, v39
	v_fmac_f32_e32 v8, v4, v40
	v_fmac_f32_e32 v8, v5, v41
	ds_read_b128 v[2:5], v17 offset:38656
	ds_read_b128 v[56:59], v17 offset:38912
	ds_read_b128 v[60:63], v17 offset:38928
	s_waitcnt lgkmcnt(3)
	v_fmac_f32_e32 v8, v44, v42
	v_fmac_f32_e32 v8, v45, v43
	s_waitcnt lgkmcnt(2)
	v_fma_f32 v9, v2, v18, 0
	v_fmac_f32_e32 v9, v3, v19
	v_fmac_f32_e32 v9, v4, v20
	v_fmac_f32_e32 v9, v5, v21
	ds_read_b128 v[2:5], v17 offset:38720
	v_fmac_f32_e32 v9, v52, v22
	v_fmac_f32_e32 v9, v53, v23
	v_fmac_f32_e32 v9, v54, v24
	v_fmac_f32_e32 v9, v55, v25
	ds_read_b128 v[52:55], v17 offset:38736
	s_waitcnt lgkmcnt(1)
	v_fmac_f32_e32 v9, v2, v26
	v_fmac_f32_e32 v9, v3, v27
	v_fmac_f32_e32 v9, v4, v28
	v_fmac_f32_e32 v9, v5, v29
	ds_read_b128 v[2:5], v17 offset:38784
	s_waitcnt lgkmcnt(1)
	v_fmac_f32_e32 v9, v52, v30
	v_fmac_f32_e32 v9, v53, v31
	v_fmac_f32_e32 v9, v54, v32
	v_fmac_f32_e32 v9, v55, v33
	ds_read_b128 v[52:55], v17 offset:38800
	s_waitcnt lgkmcnt(1)
	v_fmac_f32_e32 v9, v2, v34
	v_fmac_f32_e32 v9, v3, v35
	v_fmac_f32_e32 v9, v4, v36
	v_fmac_f32_e32 v9, v5, v37
	ds_read_b128 v[2:5], v17 offset:38848
	s_waitcnt lgkmcnt(1)
	v_fmac_f32_e32 v9, v52, v38
	v_fmac_f32_e32 v9, v53, v39
	v_fmac_f32_e32 v9, v54, v40
	v_fmac_f32_e32 v9, v55, v41
	ds_read_b128 v[52:55], v17 offset:38864
	v_fma_f32 v44, v56, v18, 0
	v_fmac_f32_e32 v44, v57, v19
	v_fmac_f32_e32 v44, v58, v20
	v_fmac_f32_e32 v44, v59, v21
	ds_read_b128 v[18:21], v17 offset:38976
	v_fmac_f32_e32 v44, v60, v22
	v_fmac_f32_e32 v44, v61, v23
	v_fmac_f32_e32 v44, v62, v24
	v_fmac_f32_e32 v44, v63, v25
	ds_read_b128 v[22:25], v17 offset:38992
	s_waitcnt lgkmcnt(1)
	v_fmac_f32_e32 v44, v18, v26
	v_fmac_f32_e32 v44, v19, v27
	v_fmac_f32_e32 v44, v20, v28
	v_fmac_f32_e32 v44, v21, v29
	ds_read_b128 v[18:21], v17 offset:39040
	s_waitcnt lgkmcnt(1)
	v_fmac_f32_e32 v44, v22, v30
	v_fmac_f32_e32 v44, v23, v31
	v_fmac_f32_e32 v44, v24, v32
	v_fmac_f32_e32 v44, v25, v33
	ds_read_b128 v[22:25], v17 offset:39056
	s_waitcnt lgkmcnt(1)
	v_fmac_f32_e32 v44, v18, v34
	v_fmac_f32_e32 v44, v19, v35
	v_fmac_f32_e32 v44, v20, v36
	v_fmac_f32_e32 v44, v21, v37
	ds_read_b128 v[18:21], v17 offset:39104
	s_waitcnt lgkmcnt(1)
; DI float half_sum(float v) { const auto rr = __builtin_amdgcn_permlane32_swap(__float_as_uint(v), __float_as_uint(v), false, false); return __uint_as_float(rr[0]) + __uint_as_float(rr[1]); }
; DI void phase_attn(Frame& F, int l) {
;     ...
; #pragma unroll
;             for (int j = 0; j < 8; ++j) { float a = 0.f;
; #pragma unroll
;                 for (int s = 0; s < 4; ++s)
; #pragma unroll
;                     for (int e = 0; e < 8; ++e) a += __uint_as_float(((unsigned)(unsigned short)qf[s][e]) << 16) * KM[j * 64 + 16 * s + 8 * hh + e];
;                 a = half_sum(a); gsc[j] = (j < qblk) ? a : -INFINITY; }
	v_fmac_f32_e32 v44, v22, v38
	v_fmac_f32_e32 v9, v2, v42
	v_fmac_f32_e32 v44, v23, v39
	v_fmac_f32_e32 v9, v3, v43
	v_fmac_f32_e32 v44, v24, v40
	v_pk_mul_f32 v[2:3], v[46:47], v[14:15]
	v_fmac_f32_e32 v44, v25, v41
	v_add_f32_e32 v2, v8, v2
	s_waitcnt lgkmcnt(0)
	v_fmac_f32_e32 v44, v18, v42
	v_add_f32_e32 v18, v2, v3
	v_pk_mul_f32 v[2:3], v[4:5], v[14:15]
	v_fmac_f32_e32 v44, v19, v43
	v_add_f32_e32 v2, v9, v2
	v_add_f32_e32 v19, v2, v3
	v_pk_mul_f32 v[2:3], v[20:21], v[14:15]
	v_pk_mul_f32 v[8:9], v[48:49], v[12:13]
	v_add_f32_e32 v2, v44, v2
	v_add_f32_e32 v14, v2, v3
	ds_read_b128 v[2:5], v17 offset:39120
	v_add_f32_e32 v8, v18, v8
	v_add_f32_e32 v15, v8, v9
	v_pk_mul_f32 v[8:9], v[52:53], v[12:13]
	s_cmp_gt_u32 s37, 2
	s_waitcnt lgkmcnt(0)
; DI float half_sum(float v) { const auto rr = __builtin_amdgcn_permlane32_swap(__float_as_uint(v), __float_as_uint(v), false, false); return __uint_as_float(rr[0]) + __uint_as_float(rr[1]); }
; DI void phase_attn(Frame& F, int l) {
;     ...
;                 a = half_sum(a); gsc[j] = (j < qblk) ? a : -INFINITY; }
; #pragma unroll
;             for (int rnd = 0; rnd < 3; ++rnd) { float bv = -INFINITY; int bi = -1;
; #pragma unroll
;                 for (int j = 0; j < 8; ++j) if (gsc[j] > bv) { bv = gsc[j]; bi = j; }
;                 if (bi >= 0) selmask |= 1u << bi;
; #pragma unroll
;                 for (int j = 0; j < 8; ++j) if (j == bi) gsc[j] = -INFINITY; }
;         }
;     ...
;         {
; #pragma unroll
;             for (int i = 0; i < 16; ++i) { o[0][i] = 0.f; o[1][i] = 0.f; }
;             l_run = 0.f;
; #pragma unroll
;             for (int i = 0; i < 16; ++i) lacc[i] = 0.f;
;             __syncthreads();
	v_pk_mul_f32 v[2:3], v[2:3], v[12:13]
	v_add_f32_e32 v8, v19, v8
	v_add_f32_e32 v2, v14, v2
	v_add_f32_e32 v8, v8, v9
	v_add_f32_e32 v9, v2, v3
	v_pk_mul_f32 v[2:3], v[50:51], v[6:7]
	s_cselect_b64 s[8:9], -1, 0
	v_add_f32_e32 v2, v15, v2
	v_add_f32_e32 v2, v2, v3
	s_cmp_gt_u32 s37, 3
	v_mov_b32_e32 v3, v2
	s_cselect_b64 s[10:11], -1, 0
	s_cmp_gt_u32 s37, 4
	v_permlane32_swap_b32_e32 v2, v3
	v_cndmask_b32_e32 v13, v205, v65, vcc
	v_add_f32_e32 v2, v2, v3
	s_cselect_b64 vcc, -1, 0
	v_cndmask_b32_e32 v15, v205, v2, vcc
	v_pk_mul_f32 v[2:3], v[54:55], v[6:7]
	s_cmp_gt_u32 s37, 6
	v_add_f32_e32 v2, v8, v2
	v_add_f32_e32 v2, v2, v3
	v_mov_b32_e32 v3, v2
	s_nop 1
	v_permlane32_swap_b32_e32 v2, v3
	v_add_f32_e32 v2, v2, v3
	v_cndmask_b32_e64 v8, v205, v2, s[6:7]
	v_pk_mul_f32 v[2:3], v[4:5], v[6:7]
	v_cndmask_b32_e64 v12, v205, v64, s[4:5]
	v_add_f32_e32 v2, v9, v2
	v_add_f32_e32 v2, v2, v3
	v_mov_b32_e32 v3, v2
	s_nop 1
	v_permlane32_swap_b32_e32 v2, v3
	v_add_f32_e32 v2, v2, v3
	s_cselect_b64 vcc, -1, 0
	v_cndmask_b32_e32 v2, v205, v2, vcc
	v_cmp_nlg_f32_e32 vcc, s60, v12
	v_cndmask_b32_e64 v14, v205, v66, s[8:9]
	v_cndmask_b32_e64 v17, v205, v67, s[10:11]
	v_cndmask_b32_e32 v4, v12, v205, vcc
	v_cndmask_b32_e64 v3, 0, -1, vcc
	v_cmp_gt_f32_e32 vcc, v13, v4
	s_lshl_b32 s39, s37, 2
	s_add_i32 s29, s39, 4
	v_cndmask_b32_e32 v4, v4, v13, vcc
	v_cndmask_b32_e64 v3, v3, 1, vcc
	v_cmp_gt_f32_e32 vcc, v14, v4
	s_min_u32 s38, s29, 6
	v_readlane_b32 s0, v253, 31
	v_cndmask_b32_e32 v4, v4, v14, vcc
	v_cndmask_b32_e64 v3, v3, 2, vcc
	v_cmp_gt_f32_e32 vcc, v17, v4
	v_readlane_b32 s1, v253, 32
	s_add_u32 s0, s0, s28
	v_cndmask_b32_e32 v4, v4, v17, vcc
	v_cndmask_b32_e64 v3, v3, 3, vcc
	v_cmp_gt_f32_e32 vcc, v15, v4
	s_addc_u32 s1, s1, 0
	v_lshl_add_u64 v[172:173], s[0:1], 0, v[0:1]
	v_cndmask_b32_e32 v4, v4, v15, vcc
	v_cndmask_b32_e64 v3, v3, 4, vcc
	v_cmp_gt_f32_e32 vcc, v8, v4
	v_readlane_b32 s0, v253, 15
	v_readlane_b32 s1, v253, 16
	v_cndmask_b32_e32 v4, v4, v8, vcc
	v_cndmask_b32_e64 v3, v3, 5, vcc
	v_cmp_gt_f32_e32 vcc, v2, v4
	s_add_u32 s0, s0, s28
	s_addc_u32 s1, s1, 0
	v_cndmask_b32_e64 v3, v3, 6, vcc
	v_lshlrev_b32_e64 v4, v3, 1
	v_cmp_lt_i32_e64 s[6:7], -1, v3
	v_cndmask_b32_e32 v2, v2, v205, vcc
	v_lshlrev_b32_e32 v190, 2, v16
	v_cndmask_b32_e64 v4, 0, v4, s[6:7]
	v_cmp_ne_u32_e64 s[6:7], 0, v3
	s_mov_b32 s17, s59
	v_lshl_add_u64 v[174:175], s[0:1], 0, v[0:1]
	v_cndmask_b32_e64 v5, v205, v12, s[6:7]
	v_cmp_ne_u32_e64 s[6:7], 1, v3
	v_cmp_nlg_f32_e32 vcc, s60, v5
	s_movk_i32 s0, 0x90
	v_cndmask_b32_e64 v6, v205, v13, s[6:7]
	v_cmp_ne_u32_e64 s[6:7], 2, v3
	v_cndmask_b32_e32 v13, v5, v205, vcc
	v_lshlrev_b32_e32 v193, 4, v16
	v_cndmask_b32_e64 v7, v205, v14, s[6:7]
	v_cmp_ne_u32_e64 s[6:7], 3, v3
	v_mov_b32_e32 v14, v1
	v_lshlrev_b32_e32 v187, 3, v186
	v_cndmask_b32_e64 v9, v205, v17, s[6:7]
	v_cmp_ne_u32_e64 s[6:7], 4, v3
	v_lshl_add_u64 v[176:177], v[10:11], 0, s[16:17]
	v_mov_b32_e32 v10, v1
	v_cndmask_b32_e64 v12, v205, v15, s[6:7]
	v_cmp_ne_u32_e64 s[6:7], 5, v3
	v_mov_b32_e32 v15, v1
	v_mov_b32_e32 v11, v1
	v_cndmask_b32_e64 v3, v205, v8, s[6:7]
	v_cndmask_b32_e64 v8, 0, -1, vcc
	v_cmp_gt_f32_e32 vcc, v6, v13
	v_mov_b32_e32 v16, 0
	s_mov_b32 s33, 0
	v_cndmask_b32_e32 v13, v13, v6, vcc
	v_cndmask_b32_e64 v8, v8, 1, vcc
	v_cmp_gt_f32_e32 vcc, v7, v13
	s_ashr_i32 s28, s97, 1
	v_and_b32_e32 v215, 24, v187
	v_cndmask_b32_e32 v13, v13, v7, vcc
	v_cndmask_b32_e64 v8, v8, 2, vcc
	v_cmp_gt_f32_e32 vcc, v9, v13
	v_mul_u32_u24_e32 v216, 0x90, v188
	v_mov_b32_e32 v17, v16
	v_cndmask_b32_e32 v13, v13, v9, vcc
	v_cndmask_b32_e64 v8, v8, 3, vcc
	v_cmp_gt_f32_e32 vcc, v12, v13
	v_mov_b32_e32 v18, v16
	v_mov_b32_e32 v19, v16
	v_cndmask_b32_e32 v13, v13, v12, vcc
	v_cndmask_b32_e64 v8, v8, 4, vcc
	v_cmp_gt_f32_e32 vcc, v3, v13
	v_mov_b32_e32 v20, v16
	v_mov_b32_e32 v21, v16
	v_cndmask_b32_e32 v13, v13, v3, vcc
	v_cndmask_b32_e64 v8, v8, 5, vcc
	v_cmp_gt_f32_e32 vcc, v2, v13
	v_mov_b32_e32 v22, v16
	v_mov_b32_e32 v23, v16
	v_cndmask_b32_e64 v8, v8, 6, vcc
	v_lshlrev_b32_e64 v13, v8, 1
	v_cmp_lt_i32_e64 s[6:7], -1, v8
	v_cndmask_b32_e32 v2, v2, v205, vcc
	v_mov_b32_e32 v24, v16
	v_cndmask_b32_e64 v13, 0, v13, s[6:7]
	v_cmp_ne_u32_e64 s[6:7], 0, v8
	v_mov_b32_e32 v25, v16
	v_mov_b32_e32 v26, v16
	v_cndmask_b32_e64 v5, v205, v5, s[6:7]
	v_cmp_ne_u32_e64 s[6:7], 1, v8
	v_cmp_nlg_f32_e32 vcc, s60, v5
	v_mov_b32_e32 v27, v16
	v_cndmask_b32_e64 v6, v205, v6, s[6:7]
	v_cmp_ne_u32_e64 s[6:7], 2, v8
	v_cndmask_b32_e32 v5, v5, v205, vcc
	v_mov_b32_e32 v28, v16
	v_cndmask_b32_e64 v7, v205, v7, s[6:7]
	v_cmp_ne_u32_e64 s[6:7], 3, v8
	v_mov_b32_e32 v29, v16
	v_mov_b32_e32 v30, v16
	v_cndmask_b32_e64 v9, v205, v9, s[6:7]
	v_cmp_ne_u32_e64 s[6:7], 4, v8
	v_mov_b32_e32 v31, v16
	v_mov_b32_e32 v32, v16
	v_cndmask_b32_e64 v12, v205, v12, s[6:7]
	v_cmp_ne_u32_e64 s[6:7], 5, v8
	v_cndmask_b32_e64 v8, 0, -1, vcc
	v_cmp_gt_f32_e32 vcc, v6, v5
	v_cndmask_b32_e64 v3, v205, v3, s[6:7]
	v_mov_b32_e32 v33, v16
	v_cndmask_b32_e32 v5, v5, v6, vcc
	v_cndmask_b32_e64 v8, v8, 1, vcc
	v_cmp_gt_f32_e32 vcc, v7, v5
	v_mov_b32_e32 v34, v16
	v_mov_b32_e32 v35, v16
	v_cndmask_b32_e32 v5, v5, v7, vcc
	v_cndmask_b32_e64 v6, v8, 2, vcc
	v_cmp_gt_f32_e32 vcc, v9, v5
	v_mov_b32_e32 v7, v1
	v_mov_b32_e32 v8, v1
	v_cndmask_b32_e32 v5, v5, v9, vcc
	v_cndmask_b32_e64 v6, v6, 3, vcc
	v_cmp_gt_f32_e32 vcc, v12, v5
	v_mov_b32_e32 v9, v1
	v_mov_b32_e32 v36, v16
	v_cndmask_b32_e32 v5, v5, v12, vcc
	v_cndmask_b32_e64 v6, v6, 4, vcc
	v_cmp_gt_f32_e32 vcc, v3, v5
	v_mov_b32_e32 v12, v1
	v_mov_b32_e32 v37, v16
	v_cndmask_b32_e32 v3, v5, v3, vcc
	v_cndmask_b32_e64 v6, v6, 5, vcc
	v_cmp_ngt_f32_e32 vcc, v2, v3
	v_mov_b32_e32 v5, v1
	v_mov_b32_e32 v38, v16
	v_cndmask_b32_e32 v2, 6, v6, vcc
	v_lshlrev_b32_e64 v3, v2, 1
	v_cmp_lt_i32_e32 vcc, -1, v2
	v_mov_b32_e32 v6, v1
	v_mov_b32_e32 v39, v16
	v_cndmask_b32_e32 v2, 0, v3, vcc
	v_lshrrev_b32_e32 v3, 2, v186
	v_or3_b32 v191, v13, v4, v2
	v_and_or_b32 v0, v3, 3, v190
	v_lshlrev_b32_e32 v2, 1, v186
	v_and_b32_e32 v214, 32, v2
	v_mul_lo_u32 v217, v0, s0
	v_mov_b32_e32 v0, v1
	v_mov_b32_e32 v2, v1
	v_mov_b32_e32 v3, v1
	v_mov_b32_e32 v4, v1
	v_mov_b32_e32 v13, v1
	v_mov_b64_e32 v[62:63], v[14:15]
	v_mov_b64_e32 v[60:61], v[12:13]
	v_mov_b64_e32 v[58:59], v[10:11]
	v_mov_b64_e32 v[56:57], v[8:9]
	v_mov_b64_e32 v[54:55], v[6:7]
	v_mov_b64_e32 v[52:53], v[4:5]
	v_mov_b64_e32 v[50:51], v[2:3]
	v_mov_b64_e32 v[48:49], v[0:1]
	v_mov_b32_e32 v40, v16
	v_mov_b32_e32 v41, v16
	v_mov_b32_e32 v42, v16
	v_mov_b32_e32 v43, v16
	v_mov_b32_e32 v44, v16
	v_mov_b32_e32 v45, v16
	v_mov_b32_e32 v46, v16
	v_mov_b32_e32 v47, v16
	s_barrier

.LBB0_504:
	s_bitcmp1_b32 s0, 0
	s_cselect_b32 s1, 0x2400, 0
	v_add_u32_e32 v0, s1, v189
	s_add_i32 s100, s0, 1
	s_cmp_ge_u32 s100, s29
	s_cbranch_scc1 .Lnadvs_tail
	s_bitcmp1_b32 s0, 0
	s_cbranch_scc1 .Lnadvs_odd
	s_waitcnt vmcnt(3)
	ds_write_b128 v0, v[206:209]
	s_waitcnt vmcnt(2)
	ds_write_b128 v0, v[210:213] offset:18432
	s_branch .Lnadv_ld
.Lnadvs_odd:
	s_waitcnt vmcnt(3)
	ds_write_b128 v0, v[160:163]
	s_waitcnt vmcnt(2)
	ds_write_b128 v0, v[164:167] offset:18432
	s_branch .Lnadv_ld
.Lnadvs_tail:
	s_waitcnt vmcnt(0)
	s_bitcmp1_b32 s0, 0
	s_cbranch_scc1 .Lnadvs_tailodd
	ds_write_b128 v0, v[206:209]
	ds_write_b128 v0, v[210:213] offset:18432
	s_branch .Lnadv_ld
.Lnadvs_tailodd:
	ds_write_b128 v0, v[160:163]
	ds_write_b128 v0, v[164:167] offset:18432
.Lnadv_ld:
	s_add_i32 s100, s0, 2
	s_cmp_ge_u32 s100, s29
	s_cbranch_scc1 .LBB0_506
	s_add_i32 s101, s100, -4
	s_ashr_i32 s101, s101, 2
	s_sub_i32 s101, s37, s101
	s_add_i32 s101, s101, -1
	s_and_b32 s6, s100, 3
	s_lshr_b32 s2, s100, 2
	s_cmp_eq_u32 s2, 1
	s_cbranch_scc0 .Lnadvl_ktok
	s_bfe_u32 s2, s100, 0x10001
	s_sub_i32 s2, 3, s2
	s_xor_b32 s6, s6, s2
.Lnadvl_ktok:
	s_lshl_b32 s101, s101, 8
	s_lshl_b32 s6, s6, 6
	s_add_u32 s2, s101, s6
	s_mov_b32 s3, 0
	v_lshl_add_u64 v[2:3], s[2:3], 0, v[176:177]
	v_lshlrev_b64 v[2:3], 10, v[2:3]
	v_lshl_add_u64 v[4:5], v[172:173], 0, v[2:3]
	v_lshl_add_u64 v[2:3], v[174:175], 0, v[2:3]
	s_bitcmp1_b32 s0, 0
	s_cbranch_scc1 .Lnadvl_ldodd
	global_load_dwordx4 v[206:209], v[4:5], off
	global_load_dwordx4 v[210:213], v[2:3], off
	s_branch .LBB0_506
.Lnadvl_ldodd:
	global_load_dwordx4 v[160:163], v[4:5], off
	global_load_dwordx4 v[164:167], v[2:3], off
	s_branch .LBB0_506

; #define LAS __attribute__((address_space(3)))
; DI void phase_attn(Frame& F, int l) {
;     ...
;             for (; ti < n_tiles; ++ti) {
;                 LAS unsigned char* KSb = KS + (ti & 1) * ATT_BUF; LAS unsigned char* VSb = VS + (ti & 1) * ATT_BUF;
;                 const int jb = ATT_JB(ti);
;                 const bool lane_sel = ((selmask >> jb) & 1u) != 0u;
;                 if (__ballot(lane_sel) != 0ull) ATT_BODY(0, (const LAS unsigned char*)RT);
;                 ATT_ADVANCE(ti);
.LBB0_509:
	s_bitcmp1_b32 s38, 0
	s_cselect_b32 s0, 0x2400, 0
	v_add_u32_e32 v14, s0, v12
	ds_read_b128 v[246:249], v14 offset:4704
	ds_read_b128 v[238:241], v14 offset:4672
	ds_read_b128 v[230:233], v14 offset:4640
	ds_read_b128 v[222:225], v14 offset:4608
	ds_read_b128 v[242:245], v14 offset:96
	ds_read_b128 v[234:237], v14 offset:64
	ds_read_b128 v[218:221], v14
	ds_read_b128 v[226:229], v14 offset:32
.Lfar_top:
	s_add_i32 s0, s38, -4
	s_lshr_b32 s1, s0, 2
	s_not_b32 s1, s1
	s_add_i32 s1, s37, s1
	v_lshrrev_b32_e32 v0, s1, v191
	v_and_b32_e32 v0, 1, v0
	v_cmp_eq_u32_e64 s[4:5], 1, v0
	v_bfe_u32 v0, v191, s1, 1
	v_cmp_ne_u32_e32 vcc, 0, v0
	s_nop 1
	s_mov_b64 s[6:7], vcc
	v_cndmask_b32_e64 v64, v250, v192, s[4:5]
	v_mov_b32_e32 v65, v64
	v_mov_b32_e32 v66, v64
	v_mov_b32_e32 v67, v64
	v_mov_b32_e32 v68, v64
	v_mov_b32_e32 v69, v64
	v_mov_b32_e32 v70, v64
	v_mov_b32_e32 v71, v64
	v_mov_b32_e32 v72, v64
	v_mov_b32_e32 v73, v64
	v_mov_b32_e32 v74, v64
	v_mov_b32_e32 v75, v64
	v_mov_b32_e32 v76, v64
	v_mov_b32_e32 v77, v64
	v_mov_b32_e32 v78, v64
	v_mov_b32_e32 v79, v64
	s_waitcnt lgkmcnt(0)
	s_add_i32 s2, s38, 1
	s_cmp_ge_u32 s2, s29
	s_cbranch_scc1 .Lfar_staged
	s_bitcmp1_b32 s2, 0
	s_cselect_b32 s0, 0x2400, 0
	v_add_u32_e32 v13, s0, v189
	s_add_i32 s100, s2, 1
	s_cmp_ge_u32 s100, s29
	s_cbranch_scc1 .Lfst_tail
	s_bitcmp1_b32 s2, 0
	s_cbranch_scc1 .Lfst_odd
	s_waitcnt vmcnt(3)
	ds_write_b128 v13, v[206:209]
	s_waitcnt vmcnt(2)
	ds_write_b128 v13, v[210:213] offset:18432
	s_branch .Lfar_staged
.Lfst_odd:
	s_waitcnt vmcnt(3)
	ds_write_b128 v13, v[160:163]
	s_waitcnt vmcnt(2)
	ds_write_b128 v13, v[164:167] offset:18432
	s_branch .Lfar_staged
.Lfst_tail:
	s_waitcnt vmcnt(0)
	s_bitcmp1_b32 s2, 0
	s_cbranch_scc1 .Lfst_tailodd
	ds_write_b128 v13, v[206:209]
	ds_write_b128 v13, v[210:213] offset:18432
	s_branch .Lfar_staged
.Lfst_tailodd:
	ds_write_b128 v13, v[160:163]
	ds_write_b128 v13, v[164:167] offset:18432
.Lfar_staged:
	s_cmp_eq_u64 s[6:7], 0
	s_cbranch_scc1 .Lfar_nobody1
	s_bitcmp1_b32 s38, 0
	s_cselect_b32 s0, 0x2400, 0
	v_add_u32_e32 v0, s0, v10
	s_mov_b32 s41, s40
	s_mov_b32 s42, s40
	s_mov_b32 s43, s40
	v_mfma_f32_32x32x16_bf16 v[80:95], v[218:221], v[156:159], v[64:79]
	ds_read_b64_tr_b16 v[2:3], v0 offset:18432
	ds_read_b64_tr_b16 v[4:5], v0 offset:19584
	v_mfma_f32_32x32x16_bf16 v[64:79], v[222:225], v[156:159], v[64:79]
	ds_read_b64_tr_b16 v[8:9], v0 offset:19648
	ds_read_b64_tr_b16 v[6:7], v0 offset:18496
	v_mfma_f32_32x32x16_bf16 v[80:95], v[226:229], v[152:155], v[80:95]
	ds_read_b64_tr_b16 v[96:97], v0 offset:20736
	ds_read_b64_tr_b16 v[98:99], v0 offset:21888
	v_mfma_f32_32x32x16_bf16 v[64:79], v[230:233], v[152:155], v[64:79]
	ds_read_b64_tr_b16 v[102:103], v0 offset:21952
	ds_read_b64_tr_b16 v[100:101], v0 offset:20800
	v_mfma_f32_32x32x16_bf16 v[80:95], v[234:237], v[148:151], v[80:95]
	ds_read_b64_tr_b16 v[104:105], v0 offset:23040
	ds_read_b64_tr_b16 v[106:107], v0 offset:24192
	v_mfma_f32_32x32x16_bf16 v[64:79], v[238:241], v[148:151], v[64:79]
	ds_read_b64_tr_b16 v[110:111], v0 offset:24256
	ds_read_b64_tr_b16 v[108:109], v0 offset:23104
	v_mfma_f32_32x32x16_bf16 v[80:95], v[242:245], v[144:147], v[80:95]
	ds_read_b64_tr_b16 v[112:113], v0 offset:25344
	ds_read_b64_tr_b16 v[114:115], v0 offset:26496
	v_mfma_f32_32x32x16_bf16 v[64:79], v[246:249], v[144:147], v[64:79]
	ds_read_b64_tr_b16 v[118:119], v0 offset:26560
	ds_read_b64_tr_b16 v[116:117], v0 offset:25408
.Lfar_nobody1:
	s_waitcnt lgkmcnt(0)
	s_barrier
	s_cmp_ge_u32 s2, s29
	s_cbranch_scc1 .Lfar_noK
	s_bitcmp1_b32 s2, 0
	s_cselect_b32 s0, 0x2400, 0
	v_add_u32_e32 v14, s0, v12
	ds_read_b128 v[246:249], v14 offset:4704
	ds_read_b128 v[238:241], v14 offset:4672
	ds_read_b128 v[230:233], v14 offset:4640
	ds_read_b128 v[222:225], v14 offset:4608
	ds_read_b128 v[242:245], v14 offset:96
	ds_read_b128 v[234:237], v14 offset:64
	ds_read_b128 v[218:221], v14
	ds_read_b128 v[226:229], v14 offset:32
.Lfar_noK:
	s_cmp_eq_u64 s[6:7], 0
	s_cbranch_scc1 .Lfar_nobody2
	s_nop 7
	v_exp_f32_e32 v0, v80
	v_exp_f32_e32 v11, v81
	v_exp_f32_e32 v13, v82
	v_exp_f32_e32 v14, v83
	v_exp_f32_e32 v15, v84
	v_exp_f32_e32 v82, v85
	v_exp_f32_e32 v83, v86
	v_exp_f32_e32 v84, v87
	v_cvt_pk_bf16_f32 v80, v0, v11
	v_cvt_pk_bf16_f32 v81, v13, v14
	v_cvt_pk_bf16_f32 v82, v15, v82
	v_cvt_pk_bf16_f32 v83, v83, v84
	v_exp_f32_e32 v0, v95
	v_exp_f32_e32 v11, v92
	v_mfma_f32_32x32x16_bf16 v[16:31], v[2:5], v[80:83], v[16:31]
	v_mov_b64_e32 v[2:3], s[40:41]
	v_mov_b64_e32 v[4:5], s[42:43]
	v_exp_f32_e32 v13, v93
	v_exp_f32_e32 v14, v94
	v_mfma_f32_32x32x16_bf16 v[32:47], v[6:9], v[80:83], v[32:47]
	v_exp_f32_e32 v6, v88
	v_exp_f32_e32 v7, v89
	v_exp_f32_e32 v8, v90
	v_exp_f32_e32 v9, v91
	v_cvt_pk_bf16_f32 v6, v6, v7
	v_cvt_pk_bf16_f32 v7, v8, v9
	v_mfma_f32_32x32x16_bf16 v[48:63], v[2:5], v[80:83], v[48:63]
	v_cvt_pk_bf16_f32 v8, v11, v13
	v_cvt_pk_bf16_f32 v9, v14, v0
	v_exp_f32_e32 v0, v64
	v_exp_f32_e32 v11, v69
	v_exp_f32_e32 v13, v70
	v_exp_f32_e32 v14, v71
	v_mfma_f32_32x32x16_bf16 v[16:31], v[96:99], v[6:9], v[16:31]
	v_mfma_f32_32x32x16_bf16 v[32:47], v[100:103], v[6:9], v[32:47]
	v_mfma_f32_32x32x16_bf16 v[48:63], v[2:5], v[6:9], v[48:63]
	v_exp_f32_e32 v6, v65
	v_exp_f32_e32 v7, v66
	v_exp_f32_e32 v8, v67
	v_exp_f32_e32 v9, v68
	v_cvt_pk_bf16_f32 v6, v0, v6
	v_exp_f32_e32 v0, v79
	v_cvt_pk_bf16_f32 v7, v7, v8
	v_cvt_pk_bf16_f32 v8, v9, v11
	v_cvt_pk_bf16_f32 v9, v13, v14
	v_exp_f32_e32 v11, v76
	v_exp_f32_e32 v13, v77
	v_mfma_f32_32x32x16_bf16 v[16:31], v[104:107], v[6:9], v[16:31]
	v_exp_f32_e32 v14, v78
	v_mfma_f32_32x32x16_bf16 v[32:47], v[108:111], v[6:9], v[32:47]
	v_mfma_f32_32x32x16_bf16 v[48:63], v[2:5], v[6:9], v[48:63]
	v_exp_f32_e32 v6, v72
	v_exp_f32_e32 v7, v73
	v_exp_f32_e32 v8, v74
	v_exp_f32_e32 v9, v75
	v_cvt_pk_bf16_f32 v6, v6, v7
	v_cvt_pk_bf16_f32 v7, v8, v9
	v_cvt_pk_bf16_f32 v8, v11, v13
	v_cvt_pk_bf16_f32 v9, v14, v0
	s_nop 1
	v_mfma_f32_32x32x16_bf16 v[16:31], v[112:115], v[6:9], v[16:31]
	v_mfma_f32_32x32x16_bf16 v[32:47], v[116:119], v[6:9], v[32:47]
	v_mfma_f32_32x32x16_bf16 v[48:63], v[2:5], v[6:9], v[48:63]
.Lfar_nobody2:
	s_cmp_ge_u32 s2, s29
	s_cbranch_scc1 .Lfar_next
	s_add_i32 s100, s2, 2
	s_cmp_ge_u32 s100, s29
	s_cbranch_scc1 .Lfar_next
	s_add_i32 s101, s100, -4
	s_ashr_i32 s101, s101, 2
	s_sub_i32 s101, s37, s101
	s_add_i32 s101, s101, -1
	s_and_b32 s3, s100, 3
	s_lshr_b32 s4, s100, 2
	s_cmp_eq_u32 s4, 1
	s_cbranch_scc0 .Lfld_ktok
	s_bfe_u32 s4, s100, 0x10001
	s_sub_i32 s4, 3, s4
	s_xor_b32 s3, s3, s4
.Lfld_ktok:
	s_lshl_b32 s101, s101, 8
	s_lshl_b32 s3, s3, 6
	s_add_u32 s4, s101, s3
	s_mov_b32 s5, 0
	v_lshl_add_u64 v[2:3], s[4:5], 0, v[176:177]
	v_lshlrev_b64 v[2:3], 10, v[2:3]
	v_lshl_add_u64 v[4:5], v[172:173], 0, v[2:3]
	v_lshl_add_u64 v[2:3], v[174:175], 0, v[2:3]
	s_bitcmp1_b32 s2, 0
	s_cbranch_scc1 .Lfld_ldodd
	global_load_dwordx4 v[206:209], v[4:5], off
	global_load_dwordx4 v[210:213], v[2:3], off
	s_branch .Lfar_next
.Lfld_ldodd:
	global_load_dwordx4 v[160:163], v[4:5], off
	global_load_dwordx4 v[164:167], v[2:3], off
.Lfar_next:
	s_add_i32 s38, s38, 1
	s_cmp_lt_u32 s38, s29
	s_cbranch_scc1 .Lfar_top

; DI unsigned pk4_fp8(float a, float b, float c, float d) { int r = 0; r = __builtin_amdgcn_cvt_pk_fp8_f32(sat8(a), sat8(b), r, false); r = __builtin_amdgcn_cvt_pk_fp8_f32(sat8(c), sat8(d), r, true); return (unsigned)r; }
; DI float half_sum(float v) { const auto rr = __builtin_amdgcn_permlane32_swap(__float_as_uint(v), __float_as_uint(v), false, false); return __uint_as_float(rr[0]) + __uint_as_float(rr[1]); }
; DI void phase_attn(Frame& F, int l) {
;     ...
;         const float ltot = half_sum(l_run); const float inv = AZ8_SCALE / ltot;
; #pragma unroll
;         for (int ds = 0; ds < 2; ++ds)
; #pragma unroll
;             for (int g4 = 0; g4 < 4; g4 += 2) {
;                 const unsigned wa = pk4_fp8(o[ds][4 * g4] * inv, o[ds][4 * g4 + 1] * inv, o[ds][4 * g4 + 2] * inv, o[ds][4 * g4 + 3] * inv), wb = pk4_fp8(o[ds][4 * g4 + 4] * inv, o[ds][4 * g4 + 5] * inv, o[ds][4 * g4 + 6] * inv, o[ds][4 * g4 + 7] * inv);
;                 const auto rr = __builtin_amdgcn_permlane32_swap(wa, wb, false, false);
;                 u32x2 w; w.x = rr[0]; w.y = rr[1];
;                 *(u32x2*)(att + qtok * D + h * HD + 32 * ds + 8 * (g4 + hh)) = w; }
;         if (!((F.bid & 1) && it == 3)) { __syncthreads(); run_items1(F, 1 + l, SLOT_ITEMS, cq); }
.LBB0_568:
	v_mov_b32_e32 v0, v11
	s_nop 1
	v_permlane32_swap_b32_e32 v11, v0
	v_add_f32_e32 v0, v11, v0
	s_mov_b32 s2, 0x41000000
	s_waitcnt vmcnt(1)
	v_div_scale_f32 v2, s[0:1], v0, v0, s2
	v_rcp_f32_e32 v3, v2
	v_readlane_b32 s0, v253, 21
	v_readlane_b32 s1, v253, 22
	s_bitcmp1_b32 s19, 0
	v_fma_f32 v4, -v2, v3, 1.0
	v_fmac_f32_e32 v3, v4, v3
	v_div_scale_f32 v4, vcc, s2, v0, s2
	v_mul_f32_e32 v5, v4, v3
	s_waitcnt vmcnt(0)
	v_fma_f32 v6, -v2, v5, v4
	v_fmac_f32_e32 v5, v6, v3
	v_fma_f32 v2, -v2, v5, v4
	v_div_fmas_f32 v2, v2, v3, v5
	v_div_fixup_f32 v0, v2, v0, s2
	v_mul_f32_e32 v2, v16, v0
	v_mul_f32_e32 v3, v17, v0
	v_med3_f32 v5, v2, s53, v204
	v_med3_f32 v3, v3, s53, v204
	v_mov_b32_e32 v2, v1
	v_cvt_pk_fp8_f32 v2, v5, v3
	v_mul_f32_e32 v4, v18, v0
	v_mul_f32_e32 v3, v19, v0
	v_med3_f32 v4, v4, s53, v204
	v_med3_f32 v3, v3, s53, v204
	v_cvt_pk_fp8_f32 v2, v4, v3 op_sel:[0,0,1]
	v_mul_f32_e32 v3, v20, v0
	v_mul_f32_e32 v4, v21, v0
	v_med3_f32 v6, v3, s53, v204
	v_med3_f32 v4, v4, s53, v204
	v_mov_b32_e32 v3, v1
	v_cvt_pk_fp8_f32 v3, v6, v4
	v_mul_f32_e32 v6, v24, v0
	v_mul_f32_e32 v7, v25, v0
	v_med3_f32 v9, v6, s53, v204
	v_med3_f32 v7, v7, s53, v204
	v_mov_b32_e32 v6, v1
	v_cvt_pk_fp8_f32 v6, v9, v7
	v_mul_f32_e32 v8, v26, v0
	v_mul_f32_e32 v7, v27, v0
	v_med3_f32 v8, v8, s53, v204
	v_med3_f32 v7, v7, s53, v204
	v_cvt_pk_fp8_f32 v6, v8, v7 op_sel:[0,0,1]
	v_mul_f32_e32 v7, v28, v0
	v_mul_f32_e32 v8, v29, v0
	v_med3_f32 v10, v7, s53, v204
	v_med3_f32 v8, v8, s53, v204
	v_mov_b32_e32 v7, v1
	v_cvt_pk_fp8_f32 v7, v10, v8
	v_mul_f32_e32 v5, v22, v0
	v_mul_f32_e32 v4, v23, v0
	v_med3_f32 v5, v5, s53, v204
	v_med3_f32 v4, v4, s53, v204
	v_mul_f32_e32 v9, v30, v0
	v_mul_f32_e32 v8, v31, v0
	v_cvt_pk_fp8_f32 v3, v5, v4 op_sel:[0,0,1]
	v_med3_f32 v9, v9, s53, v204
	v_med3_f32 v8, v8, s53, v204
	v_cvt_pk_fp8_f32 v7, v9, v8 op_sel:[0,0,1]
	v_lshl_add_u64 v[4:5], s[0:1], 0, v[170:171]
	v_lshl_add_u64 v[4:5], v[4:5], 0, s[58:59]
	v_permlane32_swap_b32_e32 v2, v3
	v_lshl_add_u64 v[4:5], v[4:5], 0, v[168:169]
	global_store_dwordx2 v[4:5], v[2:3], off
	v_permlane32_swap_b32_e32 v6, v7
	v_mul_f32_e32 v2, v32, v0
	v_mul_f32_e32 v3, v33, v0
	global_store_dwordx2 v[4:5], v[6:7], off offset:16
	v_med3_f32 v7, v2, s53, v204
	v_med3_f32 v3, v3, s53, v204
	v_mov_b32_e32 v2, v1
	v_cvt_pk_fp8_f32 v2, v7, v3
	v_mul_f32_e32 v6, v34, v0
	v_mul_f32_e32 v3, v35, v0
	v_med3_f32 v6, v6, s53, v204
	v_med3_f32 v3, v3, s53, v204
	v_cvt_pk_fp8_f32 v2, v6, v3 op_sel:[0,0,1]
	v_mul_f32_e32 v3, v36, v0
	v_mul_f32_e32 v6, v37, v0
	v_med3_f32 v8, v3, s53, v204
	v_med3_f32 v6, v6, s53, v204
	v_mov_b32_e32 v3, v1
	v_cvt_pk_fp8_f32 v3, v8, v6
	v_mul_f32_e32 v7, v38, v0
	v_mul_f32_e32 v6, v39, v0
	v_med3_f32 v7, v7, s53, v204
	v_med3_f32 v6, v6, s53, v204
	v_cvt_pk_fp8_f32 v3, v7, v6 op_sel:[0,0,1]
	v_mul_f32_e32 v6, v40, v0
	v_mul_f32_e32 v7, v41, v0
	v_med3_f32 v9, v6, s53, v204
	v_med3_f32 v7, v7, s53, v204
	v_mov_b32_e32 v6, v1
	v_cvt_pk_fp8_f32 v6, v9, v7
	v_mul_f32_e32 v8, v42, v0
	v_mul_f32_e32 v7, v43, v0
	v_med3_f32 v8, v8, s53, v204
	v_med3_f32 v7, v7, s53, v204
	v_cvt_pk_fp8_f32 v6, v8, v7 op_sel:[0,0,1]
	v_mul_f32_e32 v7, v44, v0
	v_mul_f32_e32 v8, v45, v0
	v_med3_f32 v10, v7, s53, v204
	v_med3_f32 v8, v8, s53, v204
	v_mov_b32_e32 v7, v1
	v_cvt_pk_fp8_f32 v7, v10, v8
	v_mul_f32_e32 v9, v46, v0
	v_mul_f32_e32 v0, v47, v0
	v_med3_f32 v8, v9, s53, v204
	v_med3_f32 v0, v0, s53, v204
	v_cvt_pk_fp8_f32 v7, v8, v0 op_sel:[0,0,1]
	s_cselect_b64 s[0:1], -1, 0
	s_cmp_eq_u32 s18, 3
	s_cselect_b64 s[2:3], -1, 0
	s_and_b64 s[0:1], s[2:3], s[0:1]
	v_permlane32_swap_b32_e32 v2, v3
	v_permlane32_swap_b32_e32 v6, v7
	s_and_b64 vcc, exec, s[0:1]
	global_store_dwordx2 v[4:5], v[2:3], off offset:32
	global_store_dwordx2 v[4:5], v[6:7], off offset:48
	s_cbranch_vccnz .LBB0_474
	s_mov_b64 s[6:7], s[70:71]
	s_cmp_lg_u32 s63, 8
	s_barrier
	s_cbranch_scc1 .LBB0_575
	v_mov_b32_e32 v0, 0
	s_and_saveexec_b64 s[2:3], s[4:5]
	s_cbranch_execz .LBB0_574
	s_mov_b64 s[10:11], exec
	v_mbcnt_lo_u32_b32 v0, s10, 0
	v_mbcnt_hi_u32_b32 v0, s11, v0
	v_cmp_eq_u32_e32 vcc, 0, v0
	s_and_saveexec_b64 s[8:9], vcc
	s_cbranch_execz .LBB0_573
	s_bcnt1_i32_b64 s0, s[10:11]
	s_lshl_b32 s0, s0, 3
	v_mov_b32_e32 v2, s0
	global_atomic_add v2, v1, v2, s[12:13] sc0
